# expert-weight fp8 conversion rebalanced: 12 instead of 6 items per wave moved from phase 0 into the idle workgroups of the K|V phase (two passes of the unrolled conversion block)
# speedup vs baseline: 1.0238x; 1.0238x over previous
.LBB0_36:
	s_mul_i32 s0, s38, 0xffffffa0
	s_add_i32 s0, s0, 0xd800
	s_cmp_gt_i32 s38, 64
	s_cselect_b32 s2, s0, 0xc000
	s_abs_i32 s0, s34
	v_cvt_f32_u32_e32 v1, s0
	s_sub_i32 s3, 0, s0
	s_add_i32 s1, s36, s34
	v_rcp_iflag_f32_e32 v1, v1
	s_nop 0
	v_mul_f32_e32 v1, 0x4f7ffffe, v1
	v_cvt_u32_f32_e32 v1, v1
	s_nop 0
	v_readfirstlane_b32 s4, v1
	s_mul_i32 s3, s3, s4
	s_mul_hi_u32 s3, s4, s3
	s_add_i32 s3, s4, s3
	s_mul_hi_u32 s4, s3, 0x690
	s_mul_i32 s4, s4, s0
	s_sub_i32 s4, 0x690, s4
	s_sub_i32 s5, s4, s0
	s_cmp_ge_u32 s4, s0
	s_cselect_b32 s4, s5, s4
	s_sub_i32 s5, s4, s0
	s_cmp_ge_u32 s4, s0
	s_cselect_b32 s4, s5, s4
	s_sub_i32 s1, s1, s4
	s_ashr_i32 s26, s1, 31
	s_abs_i32 s1, s1
	s_mul_hi_u32 s4, s1, s3
	s_mul_i32 s4, s4, s0
	s_sub_i32 s1, s1, s4
	s_sub_i32 s4, s1, s0
	s_cmp_ge_u32 s1, s0
	s_cselect_b32 s1, s4, s1
	s_sub_i32 s4, s1, s0
	s_cmp_ge_u32 s1, s0
	s_cselect_b32 s1, s4, s1
	s_xor_b32 s27, s1, s26
	s_sub_i32 s1, s27, s26
	s_cmp_gt_i32 s2, s1
	s_cbranch_scc0 .LBB0_38
	s_add_i32 s2, s34, s2
	s_not_b32 s5, s1
	s_add_i32 s5, s5, s2
	s_ashr_i32 s4, s34, 31
	s_ashr_i32 s2, s5, 31
	s_xor_b32 s2, s2, s4
	s_abs_i32 s4, s5
	s_mul_hi_u32 s3, s4, s3
	s_mul_i32 s5, s3, s0
	s_sub_i32 s4, s4, s5
	s_add_i32 s5, s3, 1
	s_sub_i32 s8, s4, s0
	s_cmp_ge_u32 s4, s0
	s_cselect_b32 s3, s5, s3
	s_cselect_b32 s4, s8, s4
	s_add_i32 s5, s3, 1
	s_cmp_ge_u32 s4, s0
	s_cselect_b32 s0, s5, s3
	s_xor_b32 s0, s0, s2
	s_sub_i32 s35, s0, s2

.LBB0_516:
	s_or_b64 exec, exec, s[2:3]
	s_cmpk_lt_i32 s38, 0x41
	s_cselect_b64 s[0:1], -1, 0
	s_cmp_lt_i32 s6, 64
	s_cselect_b64 s[2:3], -1, 0
	s_or_b64 s[0:1], s[2:3], s[0:1]
	s_and_b64 vcc, exec, s[0:1]
	s_cbranch_vccnz .LBB0_734
	s_mov_b32 s99, -12
.Lcv_pass:
	s_add_i32 s35, s34, 0xfffffe00
	s_lshl_b32 s0, s6, 3
	s_mul_i32 s1, s35, s99
	s_add_i32 s0, s0, s1
	s_add_i32 s53, s88, s0
	s_add_i32 s53, s53, 0xc490
	s_cmp_gt_i32 s53, 0x868f
	s_cselect_b64 s[24:25], -1, 0
	s_and_b64 vcc, exec, s[24:25]
	s_cbranch_vccnz .LBB0_519
	s_add_i32 s0, s53, 0xfffff970
	s_ashr_i32 s1, s0, 31
	s_lshr_b32 s1, s1, 22
	s_load_dwordx2 s[2:3], s[20:21], 0xd8
	s_waitcnt lgkmcnt(0)
	s_load_dwordx2 s[8:9], s[20:21], 0xf0
	s_add_i32 s1, s0, s1
	s_ashr_i32 s10, s1, 10
	s_and_b32 s1, s1, 0xfffffc00
	s_ashr_i32 s11, s10, 31
	s_sub_i32 s1, s0, s1
	s_lshl_b64 s[12:13], s[10:11], 23
	s_waitcnt lgkmcnt(0)
	s_add_u32 s8, s8, s12
	s_addc_u32 s9, s9, s13
	s_lshl_b64 s[10:11], s[10:11], 21
	s_add_u32 s0, s22, s10
	s_addc_u32 s10, s23, s11
	s_add_u32 s26, s0, 0x2400000
	s_addc_u32 s27, s10, 0
	s_movk_i32 s0, 0x800
	s_cbranch_execz .LBB0_520
	s_branch .LBB0_521

.LBB0_733:
	s_lshl_b32 s1, s0, 6
	s_lshl_b32 s0, s0, 2
	s_and_b32 s1, s1, 0x700
	s_and_b32 s0, s0, 0xffffff80
	s_add_i32 s1, s1, s0
	s_and_b32 s0, s12, 0x60
	s_or_b32 s2, s1, s0
	s_waitcnt vmcnt(0)
	v_add_u32_e32 v7, 0x2800, v10
	s_and_b64 s[0:1], exec, s[10:11]
	ds_read2_b32 v[30:31], v7 offset1:32
	v_add_u32_e32 v7, 0x2400, v10
	s_cselect_b32 s0, s12, s2
	ds_read2_b32 v[32:33], v7 offset0:192 offset1:224
	ds_read2_b32 v[34:35], v7 offset0:128 offset1:160
	ds_read2_b32 v[36:37], v7 offset0:64 offset1:96
	ds_read2_b32 v[38:39], v7 offset1:32
	v_add_u32_e32 v7, 0x2000, v10
	s_ashr_i32 s1, s0, 31
	ds_read2_b32 v[40:41], v7 offset0:192 offset1:224
	ds_read2_b32 v[42:43], v7 offset0:128 offset1:160
	ds_read2_b32 v[44:45], v7 offset0:64 offset1:96
	v_add_u32_e32 v7, 0x2800, v9
	s_lshl_b64 s[0:1], s[0:1], 10
	ds_read2_b32 v[26:27], v7 offset1:32
	v_add_u32_e32 v7, 0x2400, v9
	v_add_u32_e32 v9, 0x2000, v9
	s_add_u32 s0, s24, s0
	ds_read2_b32 v[28:29], v7 offset0:192 offset1:224
	ds_read2_b32 v[46:47], v7 offset0:128 offset1:160
	ds_read2_b32 v[48:49], v7 offset0:64 offset1:96
	ds_read2_b32 v[50:51], v9 offset0:64 offset1:96
	ds_read2_b32 v[52:53], v7 offset1:32
	ds_read2_b32 v[54:55], v9 offset0:128 offset1:160
	ds_read2_b32 v[56:57], v9 offset0:192 offset1:224
	s_addc_u32 s1, s25, s1
	s_add_u32 s0, s0, s8
	s_addc_u32 s1, s1, s9
	v_lshl_add_u64 v[58:59], s[0:1], 0, v[4:5]
	s_waitcnt lgkmcnt(3)
	v_mul_f32_e32 v4, v8, v50
	v_mul_f32_e32 v5, v6, v51
	s_waitcnt lgkmcnt(1)
	v_mul_f32_e32 v10, v11, v55
	v_mul_f32_e32 v55, v24, v26
	v_mov_b32_e32 v26, 0
	v_cvt_pk_fp8_f32 v26, v4, v5
	v_mul_f32_e32 v9, v12, v54
	v_mul_f32_e32 v5, v8, v44
	v_mul_f32_e32 v6, v6, v45
	v_mov_b32_e32 v4, 0
	s_waitcnt lgkmcnt(0)
	v_mul_f32_e32 v25, v14, v56
	v_mul_f32_e32 v50, v13, v57
	v_mul_f32_e32 v51, v16, v52
	v_mul_f32_e32 v52, v15, v53
	v_mul_f32_e32 v48, v18, v48
	v_mul_f32_e32 v49, v17, v49
	v_mul_f32_e32 v47, v19, v47
	v_mul_f32_e32 v53, v22, v28
	v_mul_f32_e32 v54, v21, v29
	v_mul_f32_e32 v56, v23, v27
	v_mov_b32_e32 v7, 0
	v_mov_b32_e32 v27, 0
	v_mov_b32_e32 v28, 0
	v_mov_b32_e32 v29, 0
	v_cvt_pk_fp8_f32 v26, v9, v10 op_sel:[0,0,1]
	v_mul_f32_e32 v9, v11, v43
	v_mul_f32_e32 v10, v14, v40
	v_mul_f32_e32 v11, v13, v41
	v_mul_f32_e32 v13, v15, v39
	v_mul_f32_e32 v14, v18, v36
	v_mul_f32_e32 v15, v17, v37
	v_mul_f32_e32 v17, v19, v35
	v_mul_f32_e32 v18, v22, v32
	v_mul_f32_e32 v19, v21, v33
	v_cvt_pk_fp8_f32 v4, v5, v6
	v_mov_b32_e32 v5, 0
	v_mov_b32_e32 v6, 0
	v_cvt_pk_fp8_f32 v27, v25, v50
	v_cvt_pk_fp8_f32 v28, v48, v49
	v_cvt_pk_fp8_f32 v29, v53, v54
	v_cvt_pk_fp8_f32 v5, v10, v11
	v_cvt_pk_fp8_f32 v6, v14, v15
	v_cvt_pk_fp8_f32 v7, v18, v19
	v_mul_f32_e32 v46, v20, v46
	v_mul_f32_e32 v8, v12, v42
	v_mul_f32_e32 v12, v16, v38
	v_mul_f32_e32 v16, v20, v34
	v_mul_f32_e32 v20, v24, v30
	v_mul_f32_e32 v21, v23, v31
	v_cvt_pk_fp8_f32 v27, v51, v52 op_sel:[0,0,1]
	v_cvt_pk_fp8_f32 v28, v46, v47 op_sel:[0,0,1]
	v_cvt_pk_fp8_f32 v29, v55, v56 op_sel:[0,0,1]
	v_cvt_pk_fp8_f32 v4, v8, v9 op_sel:[0,0,1]
	v_cvt_pk_fp8_f32 v5, v12, v13 op_sel:[0,0,1]
	v_cvt_pk_fp8_f32 v6, v16, v17 op_sel:[0,0,1]
	v_cvt_pk_fp8_f32 v7, v20, v21 op_sel:[0,0,1]
	v_lshl_add_u64 v[2:3], v[58:59], 0, v[2:3]
	v_lshl_add_u64 v[0:1], v[58:59], 0, v[0:1]
	global_store_dwordx4 v[2:3], v[26:29], off
	global_store_dwordx4 v[0:1], v[4:7], off
	s_waitcnt lgkmcnt(0)
	s_add_i32 s99, s99, 6
	s_cmp_lt_i32 s99, 0
	s_cbranch_scc0 .Lcv_done
	s_mov_b64 s[20:21], s[86:87]
	s_mov_b64 s[22:23], s[18:19]
	v_and_b32_e32 v2, 63, v156
	s_branch .Lcv_pass
.Lcv_done:
.LBB0_734:
	s_cmp_gt_i32 s91, 4
	s_cselect_b64 s[2:3], -1, 0
	s_and_b64 s[0:1], s[4:5], s[2:3]
	s_andn2_b64 vcc, exec, s[0:1]
	s_cbranch_vccnz .LBB0_790
	s_cmp_gt_u32 s80, 63
	s_waitcnt lgkmcnt(0)
	s_mov_b64 s[8:9], 0
	s_cbranch_scc1 .LBB0_737
	v_mbcnt_hi_u32_b32 v0, -1, v217
	v_cmp_eq_u32_e32 vcc, 0, v0
	s_and_b64 s[8:9], vcc, exec
